# speedup vs baseline: 1.0011x; 1.0011x over previous
.LBB4_9:
	s_or_b64 exec, exec, s[22:23]
	s_waitcnt vmcnt(1)
	v_cndmask_b32_e64 v55, v54, v52, s[0:1]
	ds_bpermute_b32 v74, v62, v55
	ds_bpermute_b32 v76, v63, v55
	ds_bpermute_b32 v82, v64, v55
	ds_bpermute_b32 v86, v65, v55
	v_cvt_f32_i32_e32 v52, v70
	s_waitcnt lgkmcnt(3)
	v_ashrrev_i32_e32 v75, 31, v74
	s_waitcnt lgkmcnt(2)
	v_ashrrev_i32_e32 v77, 31, v76
	v_lshlrev_b64 v[74:75], 8, v[74:75]
	v_lshl_add_u64 v[84:85], v[50:51], 0, v[74:75]
	v_lshlrev_b64 v[74:75], 8, v[76:77]
	s_waitcnt lgkmcnt(1)
	v_ashrrev_i32_e32 v83, 31, v82
	v_lshl_add_u64 v[88:89], v[50:51], 0, v[74:75]
	global_load_dwordx4 v[74:77], v[84:85], off
	global_load_dwordx4 v[78:81], v[88:89], off
	v_lshlrev_b64 v[82:83], 8, v[82:83]
	s_waitcnt lgkmcnt(0)
	v_ashrrev_i32_e32 v87, 31, v86
	v_lshl_add_u64 v[82:83], v[50:51], 0, v[82:83]
	v_lshlrev_b64 v[86:87], 8, v[86:87]
	global_load_dwordx4 v[82:85], v[82:83], off
	v_lshl_add_u64 v[86:87], v[50:51], 0, v[86:87]
	global_load_dwordx4 v[86:89], v[86:87], off
	s_and_saveexec_b64 s[22:23], s[0:1]
	s_waitcnt vmcnt(4)
	v_cvt_f32_i32_e32 v53, v53
	v_add_f32_e32 v53, 1.0, v53
	v_mul_f32_e32 v71, 0x4b800000, v53
	v_cmp_gt_f32_e64 s[4:5], s27, v53
	s_nop 1
	v_cndmask_b32_e64 v53, v53, v71, s[4:5]
	v_rsq_f32_e32 v53, v53
	s_nop 0
	v_mul_f32_e32 v71, 0x45800000, v53
	v_cndmask_b32_e64 v53, v53, v71, s[4:5]
	s_or_b64 exec, exec, s[22:23]
	v_add_f32_e32 v52, 1.0, v52
	v_mul_f32_e32 v71, 0x4b800000, v52
	v_cmp_gt_f32_e64 s[0:1], s27, v52
	ds_bpermute_b32 v72, v62, v53
	ds_bpermute_b32 v90, v63, v53
	v_cndmask_b32_e64 v52, v52, v71, s[0:1]
	v_rsq_f32_e32 v52, v52
	ds_bpermute_b32 v92, v64, v53
	ds_bpermute_b32 v94, v65, v53
	v_mul_f32_e32 v71, 0x45800000, v52
	v_cndmask_b32_e64 v52, v52, v71, s[0:1]
	v_cmp_lt_i32_e64 s[0:1], 4, v70
	s_waitcnt vmcnt(3) lgkmcnt(3)
	v_pk_mul_f32 v[76:77], v[72:73], v[76:77] op_sel_hi:[0,1]
	v_pk_mul_f32 v[74:75], v[72:73], v[74:75] op_sel_hi:[0,1]
	v_pk_fma_f32 v[36:37], v[36:37], v[52:53], v[76:77] op_sel_hi:[1,0,1]
	v_pk_fma_f32 v[34:35], v[34:35], v[52:53], v[74:75] op_sel_hi:[1,0,1]
	s_waitcnt vmcnt(2) lgkmcnt(2)
	v_pk_fma_f32 v[36:37], v[90:91], v[80:81], v[36:37] op_sel_hi:[0,1,1]
	v_pk_fma_f32 v[34:35], v[90:91], v[78:79], v[34:35] op_sel_hi:[0,1,1]
	s_waitcnt vmcnt(1) lgkmcnt(1)
	v_pk_fma_f32 v[36:37], v[92:93], v[84:85], v[36:37] op_sel_hi:[0,1,1]
	v_pk_fma_f32 v[74:75], v[92:93], v[82:83], v[34:35] op_sel_hi:[0,1,1]
	s_waitcnt vmcnt(0) lgkmcnt(0)
	v_pk_fma_f32 v[34:35], v[94:95], v[88:89], v[36:37] op_sel_hi:[0,1,1]
	v_pk_fma_f32 v[36:37], v[94:95], v[86:87], v[74:75] op_sel_hi:[0,1,1]
	s_and_saveexec_b64 s[4:5], s[0:1]
	s_cbranch_execz .LBB4_13
	v_min_i32_e32 v71, 16, v70
	v_add_u32_e32 v71, -4, v71
	s_mov_b64 s[22:23], 0
	v_mov_b32_e32 v72, v66
